# P0 item index remapped so both 64-byte halves of each W8 output line are written (write-through) by adjacent waves of one workgroup at the same time
# speedup vs baseline: 1.0044x; 1.0008x over previous
.LBB0_13:
	s_cmpk_gt_u32 s26, 0x4ff
	s_cbranch_scc0 .LBB0_23
	s_cmpk_gt_u32 s26, 0x84ff
	s_cbranch_scc0 .LBB0_18
	s_load_dwordx2 s[6:7], s[16:17], 0x88
	s_add_i32 s23, s26, 0xffff7b00
	s_and_b32 s50, s23, 0x1ff
	s_andn2_b32 s23, s23, 0x1ff
	s_lshr_b32 s51, s50, 6
	s_lshl_b32 s51, s51, 1
	s_and_b32 s52, s50, 1
	s_or_b32 s51, s51, s52
	s_lshl_b32 s51, s51, 5
	s_lshr_b32 s52, s50, 1
	s_and_b32 s52, s52, 0x1f
	s_or_b32 s51, s51, s52
	s_or_b32 s23, s23, s51
	s_lshr_b32 s8, s23, 9
	s_lshl_b64 s[4:5], s[8:9], 20
	s_lshl_b64 s[20:21], s[8:9], 22
	s_waitcnt lgkmcnt(0)
	s_add_u32 s6, s6, s20
	s_addc_u32 s7, s7, s21
	s_and_b32 s20, s23, 0x1ff
	s_lshl_b32 s21, s20, 5
	s_lshl_b32 s8, s23, 1
	s_and_b32 s27, s21, 0x3e0
	s_and_b32 s8, s8, 0x3c0
	v_or_b32_e32 v18, s27, v6
	s_mov_b32 s22, 1
	s_mov_b32 s23, s8
	v_mov_b32_e32 v3, v18
	s_mov_b32 s27, 0
	s_mov_b32 s28, 32

.LBB0_18:
	s_and_b64 vcc, exec, s[4:5]
	s_cbranch_vccz .LBB0_22
	s_load_dwordx2 s[6:7], s[16:17], 0x78
	s_load_dwordx2 s[4:5], s[16:17], 0x60
	s_add_i32 s22, s26, 0xfffffb00
	s_and_b32 s50, s22, 0x3ff
	s_andn2_b32 s22, s22, 0x3ff
	s_lshr_b32 s51, s50, 7
	s_lshl_b32 s51, s51, 1
	s_and_b32 s52, s50, 1
	s_or_b32 s51, s51, s52
	s_lshl_b32 s51, s51, 6
	s_lshr_b32 s52, s50, 1
	s_and_b32 s52, s52, 0x3f
	s_or_b32 s51, s51, s52
	s_or_b32 s22, s22, s51
	s_lshr_b32 s8, s22, 10
	s_lshl_b64 s[20:21], s[8:9], 23
	s_waitcnt lgkmcnt(0)
	s_add_u32 s23, s6, s20
	s_addc_u32 s21, s7, s21
	s_and_b32 s20, s22, 0x3ff
	s_and_b32 s6, s22, 0x3c0
	s_lshl_b32 s22, s22, 7
	s_lshl_b32 s7, s20, 5
	s_and_b32 s22, s22, 0x1f80
	s_add_u32 s22, s23, s22
	s_addc_u32 s23, s21, 0
	v_lshlrev_b32_e32 v12, 2, v6
	v_lshl_add_u64 v[18:19], s[22:23], 0, v[12:13]
	v_or_b32_e32 v3, s6, v1
	v_or_b32_e32 v20, s6, v4
	s_mov_b32 s21, 1
	s_mov_b32 s22, 0
	s_mov_b32 s23, 32
